# mixer phase: next-layer weight conversion shared by all 256 CUs (RWKV CUs join after their scan) instead of the 128 retention CUs; prep-wait removal and GEMM peel kept
# baseline (speedup 1.0000x reference)
.LBB0_1093:
	s_and_b64 vcc, exec, s[20:21]
	s_cbranch_vccz .LBB0_1134
	v_readlane_b32 s0, v254, 22
	s_nop 3
	s_lshl_b32 s1, s0, 3
	v_readlane_b32 s8, v255, 8
	s_add_i32 s1, s1, s8
	s_mov_b64 s[26:27], s[58:59]
	s_mov_b64 s[30:31], s[58:59]
	s_mov_b64 s[8:9], s[58:59]
	s_load_dwordx2 s[20:21], s[8:9], 0x40
	s_mov_b64 s[8:9], s[58:59]
	s_mov_b64 s[36:37], s[58:59]
	s_mov_b64 s[40:41], s[58:59]
	s_mov_b64 s[22:23], s[58:59]
	s_cmpk_gt_i32 s1, 0x19ff
	s_cbranch_scc1 .LBB0_1130
	s_load_dwordx2 s[8:9], s[26:27], 0xd8
	s_nop 0
	s_load_dwordx2 s[26:27], s[30:31], 0x108
	v_readlane_b32 s42, v255, 34
	s_load_dwordx2 s[30:31], s[36:37], 0x50
	s_nop 0
	s_load_dwordx2 s[36:37], s[40:41], 0x58
	v_readlane_b32 s43, v255, 35
	s_mul_i32 s40, s42, 0xc00000
	s_load_dwordx2 s[22:23], s[22:23], 0x60
	s_mov_b32 s43, s93
	s_mul_hi_u32 s33, s42, 0xc00000
	s_waitcnt lgkmcnt(0)
	s_add_u32 s8, s8, s40
	s_addc_u32 s9, s9, s33
	s_lshl_b64 s[40:41], s[42:43], 22
	s_mov_b32 s39, s93
	s_add_u32 s26, s26, s40
	s_addc_u32 s27, s27, s41
	s_lshl_b64 s[40:41], s[38:39], 24
	s_add_u32 s22, s22, s40
	s_addc_u32 s23, s23, s41
	s_add_u32 s36, s36, s40
	s_addc_u32 s37, s37, s41
	s_lshl_b64 s[40:41], s[38:39], 22
	s_add_u32 s30, s30, s40
	s_addc_u32 s31, s31, s41
	v_lshlrev_b32_e32 v128, 2, v64
	v_lshl_add_u64 v[32:33], s[22:23], 0, v[128:129]
	v_readlane_b32 s22, v251, 38
	v_lshl_add_u64 v[36:37], s[36:37], 0, v[128:129]
	v_readlane_b32 s36, v251, 34
	v_lshl_add_u64 v[40:41], s[30:31], 0, v[128:129]
	v_readlane_b32 s30, v251, 32
	v_lshl_add_u64 v[44:45], s[26:27], 0, v[128:129]
	v_readlane_b32 s26, v251, 26
	v_lshl_add_u64 v[48:49], s[8:9], 0, v[128:129]
	v_readlane_b32 s8, v251, 24
	v_lshlrev_b32_e32 v0, 1, v65
	v_mov_b32_e32 v1, v129
	v_readlane_b32 s23, v251, 39
	v_readlane_b32 s37, v251, 35
	v_readlane_b32 s31, v251, 33
	v_readlane_b32 s27, v251, 27
	v_readlane_b32 s9, v251, 25
	v_lshl_add_u64 v[34:35], s[22:23], 0, v[0:1]
	s_lshl_b32 s22, s38, 10
	s_mov_b32 s23, s93
	v_lshl_add_u64 v[38:39], s[36:37], 0, v[0:1]
	v_lshl_add_u64 v[42:43], s[30:31], 0, v[0:1]
	v_lshl_add_u64 v[46:47], s[26:27], 0, v[0:1]
	v_lshl_add_u64 v[50:51], s[8:9], 0, v[0:1]
	s_lshl_b32 s33, s1, 5
	s_lshl_b32 s39, s1, 1
	s_branch .LBB0_1099

.LBB0_1098:
	s_add_i32 s8, s1, 0x800
	s_add_i32 s33, s33, 0x10000
	s_addk_i32 s39, 0x1000
	s_cmpk_gt_i32 s1, 0x11ff
	s_mov_b32 s1, s8
	s_cbranch_scc1 .LBB0_1130

.LBB0_1132:
	s_mov_b64 s[8:9], s[58:59]
	s_load_dwordx2 s[8:9], s[8:9], 0x30
	v_ashrrev_i32_e32 v3, 10, v2
	v_add_u32_e32 v6, s0, v3
	v_ashrrev_i32_e32 v7, 31, v6
	v_lshl_add_u64 v[10:11], v[4:5], 0, s[30:31]
	s_waitcnt lgkmcnt(0)
	v_lshl_add_u64 v[6:7], v[6:7], 2, s[8:9]
	global_load_dword v14, v[6:7], off
	v_add_co_u32_e32 v6, vcc, 0x400000, v4
	s_mov_b32 s1, -1
	s_nop 0
	v_addc_co_u32_e32 v7, vcc, 0, v5, vcc
	global_load_dwordx4 v[6:9], v[6:7], off nt
	s_nop 0
	global_load_dwordx4 v[10:13], v[10:11], off offset:16 nt
	v_add_u32_e32 v3, 0x80000, v2
	s_mov_b64 s[8:9], 0x200000
	v_cmp_lt_i32_e32 vcc, s1, v2
	v_lshl_add_u64 v[4:5], v[4:5], 0, s[8:9]
	s_or_b64 s[20:21], vcc, s[20:21]
	v_mov_b32_e32 v2, v3
	s_waitcnt vmcnt(1)
	v_pk_mul_f32 v[8:9], v[8:9], v[14:15] op_sel_hi:[1,0]
	v_pk_mul_f32 v[6:7], v[6:7], v[14:15] op_sel_hi:[1,0]
	s_waitcnt vmcnt(0)
	v_pk_mul_f32 v[12:13], v[12:13], v[14:15] op_sel_hi:[1,0]
	v_pk_mul_f32 v[10:11], v[10:11], v[14:15] op_sel_hi:[1,0]
	v_cvt_pk_bf16_f32 v6, v6, v7
	v_cvt_pk_bf16_f32 v7, v8, v9
	v_cvt_pk_bf16_f32 v8, v10, v11
	v_cvt_pk_bf16_f32 v9, v12, v13
	global_store_dwordx4 v[0:1], v[6:9], off nt
	v_lshl_add_u64 v[0:1], v[0:1], 0, s[26:27]
	s_andn2_b64 exec, exec, s[20:21]
	s_cbranch_execnz .LBB0_1132
